# c18
# speedup vs baseline: 1.0022x; 1.0006x over previous
_Z6mxgemmILi0ELi1024ELi4EEvPKcS1_PKfS3_Pvi:
	s_load_dwordx8 s[4:11], s[0:1], 0x0
	s_lshr_b32 s13, s2, 3
	s_and_b32 s12, s2, 7
	s_lshl_b32 s12, s12, 7
	s_add_i32 s2, s12, s13
	v_readfirstlane_b32 s33, v0
	s_lshr_b32 s3, s2, 8
	s_and_b32 s2, s2, 0xff
	s_lshr_b32 s14, s2, 3
	s_and_b32 s2, s2, 7
	s_lshl_b32 s3, s3, 3
	s_add_i32 s2, s2, s3
	s_mov_b32 s15, 0
	s_mov_b32 s3, 0
	s_lshr_b32 s50, s33, 6
	s_lshr_b32 s29, s33, 8
	s_lshl_b64 s[24:25], s[14:15], 17
	s_lshl_b64 s[44:45], s[2:3], 14
	s_mul_hi_u32 s3, s33, 0xaaaaaaab
	s_lshr_b32 s30, s3, 8
	s_mul_i32 s12, s30, -6
	s_lshl_b32 s28, s50, 10
	s_add_i32 s12, s12, s50
	s_lshr_b32 s13, s3, 9
	s_bitcmp1_b32 s3, 8
	s_cselect_b32 s34, 0x3000, 0
	s_lshl_b32 s3, s12, 10
	s_add_i32 s12, s50, 8
	s_mul_hi_u32 s35, s12, 0x2aaaaaab
	s_mul_i32 s31, s13, 0x6000
	s_add_i32 s52, s3, s34
	s_lshl_b32 s3, s13, 15
	s_mul_i32 s13, s35, -6
	s_add_i32 s18, s52, s31
	s_add_i32 s13, s13, s12
	s_lshr_b32 s41, s35, 1
	s_bitcmp1_b32 s35, 0
	s_cselect_b32 s37, 0x3000, 0
	s_add_i32 s12, s50, 16
	s_lshl_b32 s42, s13, 10
	s_mul_hi_u32 s38, s12, 0x2aaaaaab
	s_mul_i32 s36, s41, 0x6000
	s_add_i32 s42, s42, s37
	s_mul_i32 s13, s38, -6
	s_add_i32 s20, s42, s36
	s_add_i32 s13, s13, s12
	s_lshr_b32 s43, s38, 1
	s_bitcmp1_b32 s38, 0
	s_cselect_b32 s40, 0x3000, 0
	s_lshl_b32 s51, s13, 10
	s_mul_i32 s39, s43, 0x6000
	s_add_i32 s51, s51, s40
	s_mul_i32 s26, s2, 0x60000
	s_add_i32 s22, s51, s39
	s_mul_hi_i32 s27, s2, 0x60000
	s_waitcnt lgkmcnt(0)
	s_add_u32 s16, s6, s44
	s_addc_u32 s17, s7, s45
	s_add_u32 s16, s16, 0xc00000
	s_addc_u32 s17, s17, 0
	s_add_u32 s12, s6, s26
	s_addc_u32 s13, s7, s27
	s_add_u32 s46, s4, s24
	s_addc_u32 s47, s5, s25
	s_add_i32 s52, s52, s3
	s_lshl_b32 s3, s41, 13
	s_add_i32 s3, s20, s3
	s_add_i32 s58, s3, 0
	s_lshl_b32 s3, s43, 13
	v_mov_b32_e32 v2, 0
	s_add_i32 s15, s28, 0
	s_add_i32 s3, s22, s3
	v_lshlrev_b32_e32 v4, 4, v0
	v_mov_b32_e32 v5, v2
	s_mov_b32 m0, s15
	s_add_i32 s59, s3, 0
	s_lshl_b32 s3, s50, 8
	v_lshl_add_u64 v[138:139], s[46:47], 0, v[4:5]
	global_load_lds_dwordx4 v4, s[46:47]
	s_mov_b64 s[46:47], 0x2000
	s_add_i32 s53, s52, 0
	s_add_i32 s3, s3, 0
	v_and_b32_e32 v1, 63, v0
	v_lshl_add_u64 v[8:9], v[138:139], 0, s[46:47]
	s_add_i32 s46, s15, 0x8000
	s_ashr_i32 s19, s18, 31
	s_add_i32 s47, s53, 0x2000
	s_ashr_i32 s21, s20, 31
	s_add_i32 s48, s58, 0x2000
	s_ashr_i32 s23, s22, 31
	s_add_i32 s49, s59, 0x2000
	s_add_i32 s50, s3, 0x20000
	v_lshlrev_b32_e32 v6, 4, v1
	v_mov_b32_e32 v7, v2
	s_add_u32 s54, s12, s18
	s_mov_b32 m0, s46
	v_lshl_add_u64 v[140:141], s[12:13], 0, v[6:7]
	s_addc_u32 s55, s13, s19
	s_addk_i32 s53, 0x3800
	global_load_lds_dwordx4 v[8:9], off
	v_lshl_add_u64 v[8:9], v[140:141], 0, s[18:19]
	s_mov_b32 m0, s47
	v_lshl_add_u64 v[132:133], s[54:55], 0, v[6:7]
	s_add_u32 s54, s12, s20
	global_load_lds_dwordx4 v[8:9], off
	v_lshl_add_u64 v[8:9], v[140:141], 0, s[20:21]
	s_mov_b32 m0, s48
	s_addc_u32 s55, s13, s21
	global_load_lds_dwordx4 v[8:9], off
	v_lshl_add_u64 v[8:9], v[140:141], 0, s[22:23]
	s_mov_b32 m0, s49
	v_lshl_add_u64 v[134:135], s[54:55], 0, v[6:7]
	s_add_i32 s55, s58, 0x3800
	v_lshlrev_b32_e32 v130, 2, v0
	global_load_lds_dwordx4 v[8:9], off
	s_mov_b32 m0, s50
	s_mov_b64 s[56:57], 0x1800
	s_add_u32 s12, s12, s22
	global_load_lds_dword v130, s[16:17]
	v_lshl_add_u64 v[8:9], v[132:133], 0, s[56:57]
	s_mov_b32 m0, s53
	s_addc_u32 s13, s13, s23
	global_load_lds_dwordx4 v[8:9], off
	v_lshl_add_u64 v[8:9], v[134:135], 0, s[56:57]
	s_mov_b32 m0, s55
	v_lshl_add_u64 v[136:137], s[12:13], 0, v[6:7]
	global_load_lds_dwordx4 v[8:9], off
	v_lshl_add_u64 v[8:9], v[136:137], 0, s[56:57]
	s_add_i32 s56, s59, 0x3800
	s_mov_b32 m0, s56
	s_load_dwordx2 s[12:13], s[0:1], 0x20
	global_load_lds_dwordx4 v[8:9], off
	s_mov_b64 s[70:71], 0x4000
	s_add_i32 m0, s28, 0x10000
	v_lshl_add_u64 v[8:9], v[138:139], 0, s[70:71]
	global_load_lds_dwordx4 v[8:9], off
	s_mov_b64 s[70:71], 0x6000
	s_add_i32 m0, s15, 0x18000
	v_lshl_add_u64 v[8:9], v[138:139], 0, s[70:71]
	global_load_lds_dwordx4 v[8:9], off
	s_cmp_lg_u32 s29, 1
	v_mov_b32_e32 v131, v2
	s_cbranch_scc1 .LBB2_2
	s_barrier

_Z6mxgemmILi1ELi4096ELi4EEvPKcS1_PKfS3_Pvi:
	s_load_dwordx4 s[4:7], s[0:1], 0x0
	s_load_dwordx2 s[10:11], s[0:1], 0x10
	s_lshr_b32 s9, s2, 3
	s_and_b32 s8, s2, 7
	s_lshl_b32 s8, s8, 6
	s_add_i32 s2, s8, s9
	v_readfirstlane_b32 s33, v0
	s_lshr_b32 s3, s2, 7
	s_and_b32 s2, s2, 0x7f
	s_lshr_b32 s12, s2, 3
	s_and_b32 s2, s2, 7
	s_lshl_b32 s8, s3, 3
	s_add_i32 s8, s8, s2
	s_mov_b32 s13, 0
	s_mov_b32 s9, 0
	s_lshr_b32 s48, s33, 6
	s_lshr_b32 s27, s33, 8
	s_lshl_b64 s[22:23], s[12:13], 19
	s_lshl_b64 s[42:43], s[8:9], 16
	s_mul_hi_u32 s2, s33, 0xaaaaaaab
	s_lshr_b32 s28, s2, 8
	s_mul_i32 s3, s28, -6
	s_lshl_b32 s26, s48, 10
	s_add_i32 s3, s3, s48
	s_lshr_b32 s9, s2, 9
	s_bitcmp1_b32 s2, 8
	s_cselect_b32 s30, 0x3000, 0
	s_lshl_b32 s2, s3, 10
	s_add_i32 s50, s2, s30
	s_add_i32 s2, s48, 8
	s_mul_hi_u32 s31, s2, 0x2aaaaaab
	s_mul_i32 s29, s9, 0x6000
	s_mul_i32 s3, s31, -6
	s_add_i32 s16, s50, s29
	s_lshl_b32 s9, s9, 15
	s_add_i32 s3, s3, s2
	s_lshr_b32 s39, s31, 1
	s_bitcmp1_b32 s31, 0
	s_cselect_b32 s35, 0x3000, 0
	s_add_i32 s2, s48, 16
	s_lshl_b32 s40, s3, 10
	s_mul_hi_u32 s36, s2, 0x2aaaaaab
	s_mul_i32 s34, s39, 0x6000
	s_add_i32 s40, s40, s35
	s_mul_i32 s3, s36, -6
	s_add_i32 s18, s40, s34
	s_add_i32 s3, s3, s2
	s_lshr_b32 s41, s36, 1
	s_bitcmp1_b32 s36, 0
	s_cselect_b32 s38, 0x3000, 0
	s_lshl_b32 s49, s3, 10
	s_mul_i32 s37, s41, 0x6000
	s_add_i32 s49, s49, s38
	s_mul_i32 s24, s8, 0x180000
	s_add_i32 s20, s49, s37
	s_mul_hi_i32 s25, s8, 0x180000
	s_waitcnt lgkmcnt(0)
	s_add_u32 s14, s6, s42
	s_addc_u32 s15, s7, s43
	s_add_u32 s14, s14, 0x3000000
	s_addc_u32 s15, s15, 0
	s_add_u32 s2, s6, s24
	s_addc_u32 s3, s7, s25
	s_add_u32 s44, s4, s22
	s_addc_u32 s45, s5, s23
	s_add_i32 s50, s50, s9
	s_lshl_b32 s9, s39, 13
	s_add_i32 s9, s18, s9
	s_add_i32 s56, s9, 0
	s_lshl_b32 s9, s41, 13
	v_mov_b32_e32 v2, 0
	s_add_i32 s13, s26, 0
	s_add_i32 s9, s20, s9
	v_lshlrev_b32_e32 v4, 4, v0
	v_mov_b32_e32 v5, v2
	s_mov_b32 m0, s13
	s_add_i32 s57, s9, 0
	s_lshl_b32 s9, s48, 8
	v_lshl_add_u64 v[138:139], s[44:45], 0, v[4:5]
	global_load_lds_dwordx4 v4, s[44:45]
	s_mov_b64 s[44:45], 0x2000
	s_add_i32 s51, s50, 0
	s_add_i32 s9, s9, 0
	v_and_b32_e32 v1, 63, v0
	v_lshl_add_u64 v[8:9], v[138:139], 0, s[44:45]
	s_add_i32 s44, s13, 0x8000
	s_ashr_i32 s17, s16, 31
	s_add_i32 s45, s51, 0x2000
	s_ashr_i32 s19, s18, 31
	s_add_i32 s46, s56, 0x2000
	s_ashr_i32 s21, s20, 31
	s_add_i32 s47, s57, 0x2000
	s_add_i32 s48, s9, 0x20000
	v_lshlrev_b32_e32 v6, 4, v1
	v_mov_b32_e32 v7, v2
	s_add_u32 s52, s2, s16
	s_mov_b32 m0, s44
	v_lshl_add_u64 v[140:141], s[2:3], 0, v[6:7]
	s_addc_u32 s53, s3, s17
	s_addk_i32 s51, 0x3800
	global_load_lds_dwordx4 v[8:9], off
	v_lshl_add_u64 v[8:9], v[140:141], 0, s[16:17]
	s_mov_b32 m0, s45
	v_lshl_add_u64 v[132:133], s[52:53], 0, v[6:7]
	s_add_u32 s52, s2, s18
	global_load_lds_dwordx4 v[8:9], off
	v_lshl_add_u64 v[8:9], v[140:141], 0, s[18:19]
	s_mov_b32 m0, s46
	s_addc_u32 s53, s3, s19
	global_load_lds_dwordx4 v[8:9], off
	v_lshl_add_u64 v[8:9], v[140:141], 0, s[20:21]
	s_mov_b32 m0, s47
	v_lshl_add_u64 v[134:135], s[52:53], 0, v[6:7]
	s_add_i32 s53, s56, 0x3800
	v_lshlrev_b32_e32 v130, 2, v0
	global_load_lds_dwordx4 v[8:9], off
	s_mov_b32 m0, s48
	s_mov_b64 s[54:55], 0x1800
	s_add_u32 s2, s2, s20
	global_load_lds_dword v130, s[14:15]
	v_lshl_add_u64 v[8:9], v[132:133], 0, s[54:55]
	s_mov_b32 m0, s51
	s_addc_u32 s3, s3, s21
	global_load_lds_dwordx4 v[8:9], off
	v_lshl_add_u64 v[8:9], v[134:135], 0, s[54:55]
	s_mov_b32 m0, s53
	v_lshl_add_u64 v[136:137], s[2:3], 0, v[6:7]
	global_load_lds_dwordx4 v[8:9], off
	v_lshl_add_u64 v[8:9], v[136:137], 0, s[54:55]
	s_add_i32 s54, s57, 0x3800
	s_mov_b32 m0, s54
	s_load_dwordx2 s[2:3], s[0:1], 0x20
	global_load_lds_dwordx4 v[8:9], off
	s_mov_b64 s[70:71], 0x4000
	s_add_i32 m0, s26, 0x10000
	v_lshl_add_u64 v[8:9], v[138:139], 0, s[70:71]
	global_load_lds_dwordx4 v[8:9], off
	s_mov_b64 s[70:71], 0x6000
	s_add_i32 m0, s13, 0x18000
	v_lshl_add_u64 v[8:9], v[138:139], 0, s[70:71]
	global_load_lds_dwordx4 v[8:9], off
	s_cmp_lg_u32 s27, 1
	v_mov_b32_e32 v131, v2
	s_cbranch_scc1 .LBB3_2
	s_barrier
